# grid barrier: the first workgroup of each XCD to arrive issues an early L2 writeback so the XCD leader's release flush has less dirty data left
# speedup vs baseline: 1.0009x; 1.0009x over previous
.LBB0_125:
	s_or_b64 exec, exec, s[6:7]
	v_cvt_f32_u32_e32 v5, v3
	s_waitcnt vmcnt(0)
	v_readfirstlane_b32 s4, v4
	v_sub_u32_e32 v4, 0, v3
	v_rcp_iflag_f32_e32 v5, v5
	v_add_u32_e32 v6, s4, v2
	v_mul_f32_e32 v5, 0x4f7ffffe, v5
	v_cvt_u32_f32_e32 v5, v5
	v_mul_lo_u32 v2, v4, v5
	v_mul_hi_u32 v2, v5, v2
	v_add_u32_e32 v2, v5, v2
	v_mul_hi_u32 v2, v6, v2
	v_mul_lo_u32 v4, v2, v3
	v_sub_u32_e32 v4, v6, v4
	v_add_u32_e32 v5, 1, v2
	v_cmp_ge_u32_e32 vcc, v4, v3
	s_nop 1
	v_cndmask_b32_e32 v2, v2, v5, vcc
	v_sub_u32_e32 v5, v4, v3
	v_cndmask_b32_e32 v4, v4, v5, vcc
	v_add_u32_e32 v5, 1, v2
	v_cmp_ge_u32_e32 vcc, v4, v3
	v_add_u32_e32 v4, 1, v6
	s_nop 0
	v_cndmask_b32_e32 v2, v2, v5, vcc
	v_mul_lo_u32 v5, v3, v2
	v_readfirstlane_b32 s8, v5
	v_readfirstlane_b32 s9, v6
	s_cmp_lg_u32 s8, s9
	s_cbranch_scc1 .Lbw_0
	buffer_wbl2 sc1
.Lbw_0:
	v_add_u32_e32 v3, v5, v3
	v_cmp_ne_u32_e32 vcc, v4, v3
	s_and_saveexec_b64 s[4:5], vcc
	s_xor_b64 s[4:5], exec, s[4:5]
	s_cbranch_execz .LBB0_139
	s_add_i32 s6, s3, 0x900
	s_mov_b32 s7, 0
	s_lshl_b64 s[6:7], s[6:7], 2
	s_add_u32 s8, s54, s6
	s_addc_u32 s9, s55, s7
	s_waitcnt lgkmcnt(0)
	v_mov_b32_e32 v1, 0
	global_load_dword v3, v1, s[8:9] sc1
	s_waitcnt vmcnt(0)
	v_cmp_eq_u32_e32 vcc, v3, v2
	s_and_saveexec_b64 s[6:7], vcc
	s_cbranch_execz .LBB0_138
	s_mov_b32 s20, 1
	s_mov_b64 s[10:11], 0
	s_branch .LBB0_129

.LBB0_224:
	s_or_b64 exec, exec, s[6:7]
	v_cvt_f32_u32_e32 v6, v4
	s_waitcnt vmcnt(0)
	v_readfirstlane_b32 s4, v5
	v_sub_u32_e32 v5, 0, v4
	v_rcp_iflag_f32_e32 v6, v6
	v_add_u32_e32 v7, s4, v3
	v_mul_f32_e32 v6, 0x4f7ffffe, v6
	v_cvt_u32_f32_e32 v6, v6
	v_mul_lo_u32 v3, v5, v6
	v_mul_hi_u32 v3, v6, v3
	v_add_u32_e32 v3, v6, v3
	v_mul_hi_u32 v3, v7, v3
	v_mul_lo_u32 v5, v3, v4
	v_sub_u32_e32 v5, v7, v5
	v_add_u32_e32 v6, 1, v3
	v_cmp_ge_u32_e32 vcc, v5, v4
	s_nop 1
	v_cndmask_b32_e32 v3, v3, v6, vcc
	v_sub_u32_e32 v6, v5, v4
	v_cndmask_b32_e32 v5, v5, v6, vcc
	v_add_u32_e32 v6, 1, v3
	v_cmp_ge_u32_e32 vcc, v5, v4
	v_add_u32_e32 v5, 1, v7
	s_nop 0
	v_cndmask_b32_e32 v3, v3, v6, vcc
	v_mul_lo_u32 v6, v4, v3
	v_readfirstlane_b32 s8, v6
	v_readfirstlane_b32 s9, v7
	s_cmp_lg_u32 s8, s9
	s_cbranch_scc1 .Lbw_1
	buffer_wbl2 sc1
.Lbw_1:
	v_add_u32_e32 v4, v6, v4
	v_cmp_ne_u32_e32 vcc, v5, v4
	s_and_saveexec_b64 s[4:5], vcc
	s_xor_b64 s[4:5], exec, s[4:5]
	s_cbranch_execz .LBB0_238
	s_add_i32 s6, s20, 0x900
	s_mov_b32 s7, s56
	s_lshl_b64 s[6:7], s[6:7], 2
	s_add_u32 s8, s54, s6
	s_addc_u32 s9, s55, s7
	s_waitcnt lgkmcnt(0)
	global_load_dword v2, v227, s[8:9] sc1
	s_waitcnt vmcnt(0)
	v_cmp_eq_u32_e32 vcc, v2, v3
	s_and_saveexec_b64 s[6:7], vcc
	s_cbranch_execz .LBB0_237
	s_mov_b32 s21, 1
	s_mov_b64 s[10:11], 0
	s_branch .LBB0_228
